# cross-attention: next chunk's query-fragment quads requested inside the MFMA body as each quad dies (was at the chunk head, needed right behind its barrier)
# speedup vs baseline: 1.0174x; 1.0033x over previous
; #define LAS __attribute__((address_space(3)))
; __device__ __forceinline__ int fresh_tid() { int t = threadIdx.x; asm volatile("" : "+v"(t)); return t; }
; template <int ROWS, int COLS> __device__ __forceinline__ void stage_load(u32x4 (&v)[ROWS * (COLS / 8) / NTHR], const bf16_t* src, size_t ld, int tid) {
;     constexpr int CPR = COLS / 8, NI = ROWS * CPR / NTHR;
; #pragma unroll
;     for (int i = 0; i < NI; ++i) { const int idx = tid + i * NTHR, r = idx / CPR, c = idx % CPR; v[i] = *(const u32x4*)(src + (size_t)r * ld + c * 8); }
; }
; template <int ROWS, int COLS, int PAD> __device__ __forceinline__ void stage_store(LAS unsigned char* dst, const u32x4 (&v)[ROWS * (COLS / 8) / NTHR], int tid) {
;     constexpr int CPR = COLS / 8, NI = ROWS * CPR / NTHR, RS = (COLS + PAD) * 2;
; #pragma unroll
;     for (int i = 0; i < NI; ++i) { const int idx = tid + i * NTHR, r = idx / CPR, c = idx % CPR; *(LAS u32x4*)(dst + r * RS + c * 16) = v[i]; }
; }
; __device__ __forceinline__ void xattn_unit(LAS unsigned char* lds, int hd, int qt, const bf16_t* QX, const bf16_t* KX, const bf16_t* VX, bf16_t* O) {
;     ...
;     const int tid = fresh_tid(), lane = tid & 63, wave = __builtin_amdgcn_readfirstlane(tid >> 6), fr = lane & 15, fq = lane >> 4;
;     LAS unsigned char* X = lds; LAS unsigned char* Pw = lds + XBYTES + wave * 16 * PRS;
;     const size_t trow = (size_t)qt * 128 + 16 * wave + fr;
;     f32x4 S[16];
; #pragma unroll
;     for (int j = 0; j < 16; ++j) S[j] = (f32x4){0.f, 0.f, 0.f, 0.f};
;     u32x4 pf[8];
;     stage_load<NMEM, 128>(pf, KX + hd * XD, D, tid);
.LBB0_978:
	v_mov_b32_e32 v198, v0
	s_lshl_b32 s10, s29, 1
	s_and_b32 s33, s10, 0xc00
	v_readfirstlane_b32 s11, v198
	s_ashr_i32 s10, s20, 2
	s_ashr_i32 s11, s11, 2
	s_and_b32 s13, s11, -16
	s_ashr_i32 s11, s10, 31
	s_ashr_i32 s12, s13, 31
	s_lshl_b64 s[10:11], s[10:11], 7
	s_waitcnt vmcnt(0)
	v_ashrrev_i32_e32 v2, 31, v198
	s_add_u32 s14, s10, s13
	v_lshrrev_b32_e32 v2, 28, v2
	s_addc_u32 s15, s11, s12
	s_lshl_b32 s10, s20, 9
	v_add_u32_e32 v2, v198, v2
	s_and_b32 s12, s10, 0x600
	v_ashrrev_i32_e32 v116, 4, v2
	v_and_b32_e32 v2, -16, v2
	s_lshl_b32 s10, s12, 1
	v_sub_u32_e32 v54, v198, v2
	s_add_u32 s10, s22, s10
	v_ashrrev_i32_e32 v117, 31, v116
	v_lshlrev_b32_e32 v126, 3, v54
	s_addc_u32 s11, s23, 0
	v_lshlrev_b64 v[124:125], 12, v[116:117]
	v_ashrrev_i32_e32 v127, 31, v126
	v_lshl_add_u64 v[2:3], s[10:11], 0, v[124:125]
	v_lshlrev_b64 v[34:35], 1, v[126:127]
	v_lshl_add_u64 v[10:11], v[2:3], 0, v[34:35]
	v_add_u32_e32 v2, 0x200, v198
	v_ashrrev_i32_e32 v3, 31, v2
	v_lshrrev_b32_e32 v3, 28, v3
	v_add_u32_e32 v3, v2, v3
	v_ashrrev_i32_e32 v118, 4, v3
	v_and_b32_e32 v3, -16, v3
	v_sub_u32_e32 v55, v2, v3
	v_ashrrev_i32_e32 v119, 31, v118
	v_lshlrev_b32_e32 v132, 3, v55
	v_lshlrev_b64 v[130:131], 12, v[118:119]
	v_ashrrev_i32_e32 v133, 31, v132
	v_lshl_add_u64 v[2:3], s[10:11], 0, v[130:131]
	v_lshlrev_b64 v[36:37], 1, v[132:133]
	v_lshl_add_u64 v[12:13], v[2:3], 0, v[36:37]
	global_load_dwordx4 v[2:5], v[10:11], off
	global_load_dwordx4 v[6:9], v[12:13], off
	v_add_u32_e32 v10, 0x400, v198
	v_ashrrev_i32_e32 v11, 31, v10
	v_lshrrev_b32_e32 v11, 28, v11
	v_add_u32_e32 v11, v10, v11
	v_ashrrev_i32_e32 v120, 4, v11
	v_and_b32_e32 v11, -16, v11
	v_sub_u32_e32 v56, v10, v11
	v_ashrrev_i32_e32 v121, 31, v120
	v_lshlrev_b32_e32 v138, 3, v56
	v_lshlrev_b64 v[136:137], 12, v[120:121]
	v_ashrrev_i32_e32 v139, 31, v138
	v_lshl_add_u64 v[10:11], s[10:11], 0, v[136:137]
	v_lshlrev_b64 v[38:39], 1, v[138:139]
	v_lshl_add_u64 v[18:19], v[10:11], 0, v[38:39]
	v_add_u32_e32 v10, 0x600, v198
	v_ashrrev_i32_e32 v11, 31, v10
	v_lshrrev_b32_e32 v11, 28, v11
	v_add_u32_e32 v11, v10, v11
	v_ashrrev_i32_e32 v122, 4, v11
	v_and_b32_e32 v11, -16, v11
	v_sub_u32_e32 v57, v10, v11
	v_ashrrev_i32_e32 v123, 31, v122
	v_lshlrev_b32_e32 v144, 3, v57
	v_lshlrev_b64 v[142:143], 12, v[122:123]
	v_ashrrev_i32_e32 v145, 31, v144
	v_lshl_add_u64 v[10:11], s[10:11], 0, v[142:143]
	v_lshlrev_b64 v[40:41], 1, v[144:145]
	v_lshl_add_u64 v[20:21], v[10:11], 0, v[40:41]
	global_load_dwordx4 v[10:13], v[18:19], off
	global_load_dwordx4 v[14:17], v[20:21], off
	v_add_u32_e32 v18, 0x800, v198
	v_ashrrev_i32_e32 v19, 31, v18
	v_lshrrev_b32_e32 v19, 28, v19
	v_add_u32_e32 v19, v18, v19
	v_ashrrev_i32_e32 v128, 4, v19
	v_and_b32_e32 v19, -16, v19
	v_sub_u32_e32 v58, v18, v19
	v_ashrrev_i32_e32 v129, 31, v128
	v_lshlrev_b32_e32 v150, 3, v58
	v_lshlrev_b64 v[148:149], 12, v[128:129]
	v_ashrrev_i32_e32 v151, 31, v150
	v_lshl_add_u64 v[18:19], s[10:11], 0, v[148:149]
	v_lshlrev_b64 v[42:43], 1, v[150:151]
	v_lshl_add_u64 v[26:27], v[18:19], 0, v[42:43]
	v_add_u32_e32 v18, 0xa00, v198
	v_ashrrev_i32_e32 v19, 31, v18
	v_lshrrev_b32_e32 v19, 28, v19
	v_add_u32_e32 v19, v18, v19
	v_ashrrev_i32_e32 v134, 4, v19
	v_and_b32_e32 v19, -16, v19
	v_sub_u32_e32 v59, v18, v19
	v_ashrrev_i32_e32 v135, 31, v134
	v_lshlrev_b32_e32 v158, 3, v59
	v_lshlrev_b64 v[156:157], 12, v[134:135]
	v_ashrrev_i32_e32 v159, 31, v158
	v_lshl_add_u64 v[18:19], s[10:11], 0, v[156:157]
	v_lshlrev_b64 v[44:45], 1, v[158:159]
	v_lshl_add_u64 v[28:29], v[18:19], 0, v[44:45]
	global_load_dwordx4 v[18:21], v[26:27], off
	global_load_dwordx4 v[22:25], v[28:29], off
	v_add_u32_e32 v26, 0xc00, v198
	v_ashrrev_i32_e32 v27, 31, v26
	v_lshrrev_b32_e32 v27, 28, v27
	v_add_u32_e32 v27, v26, v27
	v_ashrrev_i32_e32 v140, 4, v27
	v_and_b32_e32 v27, -16, v27
	v_sub_u32_e32 v60, v26, v27
	v_ashrrev_i32_e32 v141, 31, v140
	v_lshlrev_b32_e32 v164, 3, v60
	v_lshlrev_b64 v[162:163], 12, v[140:141]
	v_ashrrev_i32_e32 v165, 31, v164
	v_lshl_add_u64 v[26:27], s[10:11], 0, v[162:163]
	v_lshlrev_b64 v[46:47], 1, v[164:165]
	v_lshl_add_u64 v[48:49], v[26:27], 0, v[46:47]
	v_add_u32_e32 v26, 0xe00, v198
	v_ashrrev_i32_e32 v27, 31, v26
	v_lshrrev_b32_e32 v27, 28, v27
	v_add_u32_e32 v27, v26, v27
	v_ashrrev_i32_e32 v146, 4, v27
	v_and_b32_e32 v27, -16, v27
	v_sub_u32_e32 v61, v26, v27
	v_ashrrev_i32_e32 v147, 31, v146
	v_lshlrev_b32_e32 v176, 3, v61
	v_lshlrev_b64 v[174:175], 12, v[146:147]
	v_ashrrev_i32_e32 v177, 31, v176
	v_lshl_add_u64 v[26:27], s[10:11], 0, v[174:175]
	v_lshlrev_b64 v[50:51], 1, v[176:177]
	v_lshl_add_u64 v[52:53], v[26:27], 0, v[50:51]
	global_load_dwordx4 v[26:29], v[48:49], off
	global_load_dwordx4 v[30:33], v[52:53], off
	v_mul_lo_u32 v48, v116, s31
	v_add_u32_e32 v52, s17, v48
	v_mul_lo_u32 v48, v118, s31
	v_add_u32_e32 v53, s17, v48
	v_mul_lo_u32 v48, v120, s31
	v_lshlrev_b32_e32 v117, 4, v54
	v_add_u32_e32 v54, s17, v48
	v_mul_lo_u32 v48, v122, s31
	v_lshlrev_b32_e32 v119, 4, v55
	v_add_u32_e32 v55, s17, v48
	v_mul_lo_u32 v48, v128, s31
	v_lshlrev_b32_e32 v121, 4, v56
	v_add_u32_e32 v56, s17, v48
	v_mul_lo_u32 v48, v134, s31
	v_lshlrev_b32_e32 v123, 4, v57
	v_add_u32_e32 v57, s17, v48
	v_mul_lo_u32 v48, v140, s31
	v_and_b32_e32 v114, 15, v198
	v_lshlrev_b32_e32 v129, 4, v58
	v_add_u32_e32 v58, s17, v48
	v_mul_lo_u32 v48, v146, s31
	v_lshlrev_b32_e32 v135, 4, v59
	v_add_u32_e32 v59, s17, v48
	v_and_b32_e32 v199, 48, v198
	v_mul_u32_u24_e32 v48, 0x110, v114
	v_add3_u32 v200, s17, v199, v48
	v_or_b32_e32 v48, s33, v124
	v_mov_b32_e32 v49, v125
	v_lshl_add_u64 v[152:153], v[48:49], 0, v[34:35]
	v_or_b32_e32 v34, s33, v130
; #define MFMA16(b, a, c) __builtin_amdgcn_mfma_f32_16x16x32_bf16((b), (a), (c), 0, 0, 0)
; __device__ __forceinline__ void xattn_unit(LAS unsigned char* lds, int hd, int qt, const bf16_t* QX, const bf16_t* KX, const bf16_t* VX, bf16_t* O) {
;     ...
;     f32x4 S[16];
; #pragma unroll
;     for (int j = 0; j < 16; ++j) S[j] = (f32x4){0.f, 0.f, 0.f, 0.f};
;     u32x4 pf[8];
;     stage_load<NMEM, 128>(pf, KX + hd * XD, D, tid);
; #pragma unroll 1
;     for (int kc = 0; kc < 4; ++kc) {
;         __syncthreads();
;         stage_store<NMEM, 128, 8>(X, pf, tid);
;         bf16x8 aq[4];
; #pragma unroll
;         for (int ks = 0; ks < 4; ++ks) aq[ks] = *(const bf16x8*)(QX + trow * D + hd * XD + kc * 128 + 32 * ks + 8 * fq);
;         if (kc < 3) stage_load<NMEM, 128>(pf, KX + hd * XD + (kc + 1) * 128, D, tid);
;         __syncthreads();
; #pragma unroll
;         for (int ks = 0; ks < 4; ++ks)
; #pragma unroll
;             for (int j = 0; j < 16; ++j) S[j] = MFMA16(row_frag(X, (128 + 8) * 2, 16 * j, 32 * ks, lane), aq[ks], S[j]);
	v_mov_b32_e32 v35, v131
	v_lshl_add_u64 v[154:155], v[34:35], 0, v[36:37]
	v_or_b32_e32 v34, s14, v114
	v_mov_b32_e32 v35, s15
	v_lshlrev_b64 v[34:35], 12, v[34:35]
	v_or3_b32 v34, v34, s33, v199
	v_lshl_add_u64 v[184:185], s[6:7], 0, v[34:35]
	v_or_b32_e32 v34, s33, v136
	v_mov_b32_e32 v35, v137
	v_lshl_add_u64 v[160:161], v[34:35], 0, v[38:39]
	v_or_b32_e32 v34, s33, v174
	v_mov_b32_e32 v35, v175
	v_lshl_add_u64 v[166:167], v[34:35], 0, v[50:51]
	v_or_b32_e32 v34, s33, v162
	v_mov_b32_e32 v35, v163
	v_lshl_add_u64 v[168:169], v[34:35], 0, v[46:47]
	v_or_b32_e32 v34, s33, v156
	v_mov_b32_e32 v35, v157
	v_lshl_add_u64 v[170:171], v[34:35], 0, v[44:45]
	v_or_b32_e32 v34, s33, v148
	v_mov_b32_e32 v35, v149
	v_lshl_add_u64 v[172:173], v[34:35], 0, v[42:43]
	v_or_b32_e32 v34, s33, v142
	v_mov_b32_e32 v35, v143
	v_lshlrev_b32_e32 v141, 4, v60
	v_lshlrev_b32_e32 v147, 4, v61
	v_lshl_add_u64 v[178:179], v[34:35], 0, v[40:41]
	v_lshl_add_u64 v[180:181], s[4:5], 0, v[152:153]
	v_lshl_add_u64 v[182:183], s[4:5], 0, v[154:155]
	v_lshl_add_u64 v[186:187], s[4:5], 0, v[160:161]
	v_lshl_add_u64 v[188:189], s[4:5], 0, v[166:167]
	v_lshl_add_u64 v[190:191], s[4:5], 0, v[168:169]
	v_lshl_add_u64 v[192:193], s[4:5], 0, v[170:171]
	v_lshl_add_u64 v[194:195], s[4:5], 0, v[172:173]
	v_lshl_add_u64 v[196:197], s[4:5], 0, v[178:179]
	s_mov_b64 s[10:11], 0
	v_add_u32_e32 v201, v52, v117
	v_add_u32_e32 v202, v53, v119
	v_add_u32_e32 v203, v54, v121
	v_add_u32_e32 v204, v55, v123
	v_add_u32_e32 v205, v56, v129
	v_add_u32_e32 v206, v57, v135
	v_add_u32_e32 v207, v58, v141
	v_add_u32_e32 v208, v59, v147
	v_mov_b32_e32 v82, 0
	v_mov_b32_e32 v83, v115
	v_mov_b32_e32 v84, v115
	v_mov_b32_e32 v85, v115
	v_mov_b32_e32 v86, 0
	v_mov_b32_e32 v87, v115
	v_mov_b32_e32 v88, v115
	v_mov_b32_e32 v89, v115
	v_mov_b32_e32 v90, 0
	v_mov_b32_e32 v91, v115
	v_mov_b32_e32 v92, v115
	v_mov_b32_e32 v93, v115
	v_mov_b32_e32 v94, 0
	v_mov_b32_e32 v95, v115
	v_mov_b32_e32 v96, v115
	v_mov_b32_e32 v97, v115
	v_mov_b32_e32 v78, 0
	v_mov_b32_e32 v79, v115
	v_mov_b32_e32 v80, v115
	v_mov_b32_e32 v81, v115
	v_mov_b32_e32 v74, 0
	v_mov_b32_e32 v75, v115
	v_mov_b32_e32 v76, v115
	v_mov_b32_e32 v77, v115
	v_mov_b32_e32 v70, 0
	v_mov_b32_e32 v71, v115
	v_mov_b32_e32 v72, v115
	v_mov_b32_e32 v73, v115
	v_mov_b32_e32 v66, 0
	v_mov_b32_e32 v67, v115
	v_mov_b32_e32 v68, v115
	v_mov_b32_e32 v69, v115
	v_mov_b32_e32 v62, 0
	v_mov_b32_e32 v63, v115
	v_mov_b32_e32 v64, v115
	v_mov_b32_e32 v65, v115
	v_mov_b32_e32 v58, 0
	v_mov_b32_e32 v59, v115
	v_mov_b32_e32 v60, v115
	v_mov_b32_e32 v61, v115
	v_mov_b32_e32 v54, 0
	v_mov_b32_e32 v55, v115
	v_mov_b32_e32 v56, v115
	v_mov_b32_e32 v57, v115
	v_mov_b32_e32 v50, 0
	v_mov_b32_e32 v51, v115
	v_mov_b32_e32 v52, v115
	v_mov_b32_e32 v53, v115
	v_mov_b32_e32 v46, 0
	v_mov_b32_e32 v47, v115
	v_mov_b32_e32 v48, v115
	v_mov_b32_e32 v49, v115
	v_mov_b32_e32 v42, 0
	v_mov_b32_e32 v43, v115
	v_mov_b32_e32 v44, v115
	v_mov_b32_e32 v45, v115
	v_mov_b32_e32 v38, 0
	v_mov_b32_e32 v39, v115
	v_mov_b32_e32 v40, v115
	v_mov_b32_e32 v41, v115
	v_mov_b32_e32 v34, 0
	v_mov_b32_e32 v35, v115
	v_mov_b32_e32 v36, v115
	v_mov_b32_e32 v37, v115
	v_lshl_add_u64 v[98:99], v[184:185], 0, s[10:11]
	global_load_dwordx4 v[110:113], v[98:99], off offset:-128
	global_load_dwordx4 v[106:109], v[98:99], off offset:-64
	global_load_dwordx4 v[102:105], v[98:99], off
	s_nop 0
	global_load_dwordx4 v[98:101], v[98:99], off offset:64
	s_branch .LBB0_980
.LBB0_979:
	s_waitcnt lgkmcnt(0)
	s_barrier
	s_add_u32 s10, s10, 0x100
	s_addc_u32 s11, s11, 0
	s_cmpk_lg_i32 s10, 0x400
	ds_read_b128 v[210:213], v200
	ds_read_b128 v[214:217], v200 offset:4352
	ds_read_b128 v[228:231], v200 offset:8704
	ds_read_b128 v[232:235], v200 offset:13056
	ds_read_b128 v[236:239], v200 offset:17408
	ds_read_b128 v[240:243], v200 offset:21760
	ds_read_b128 v[244:247], v200 offset:26112
	s_waitcnt lgkmcnt(6)
	s_waitcnt vmcnt(11)
	v_mfma_f32_16x16x32_bf16 v[94:97], v[210:213], v[110:113], v[94:97]
	ds_read_b128 v[210:213], v200 offset:30464
	s_waitcnt lgkmcnt(6)
	v_mfma_f32_16x16x32_bf16 v[90:93], v[214:217], v[110:113], v[90:93]
	ds_read_b128 v[214:217], v200 offset:34816
	s_waitcnt lgkmcnt(6)
	v_mfma_f32_16x16x32_bf16 v[86:89], v[228:231], v[110:113], v[86:89]
	ds_read_b128 v[228:231], v200 offset:39168
	s_waitcnt lgkmcnt(6)
	v_mfma_f32_16x16x32_bf16 v[82:85], v[232:235], v[110:113], v[82:85]
	ds_read_b128 v[232:235], v200 offset:43520
	s_waitcnt lgkmcnt(6)
	v_mfma_f32_16x16x32_bf16 v[78:81], v[236:239], v[110:113], v[78:81]
	ds_read_b128 v[236:239], v200 offset:47872
	s_waitcnt lgkmcnt(6)
	v_mfma_f32_16x16x32_bf16 v[74:77], v[240:243], v[110:113], v[74:77]
	ds_read_b128 v[240:243], v200 offset:52224
	s_waitcnt lgkmcnt(6)
	v_mfma_f32_16x16x32_bf16 v[70:73], v[244:247], v[110:113], v[70:73]
	ds_read_b128 v[244:247], v200 offset:56576
	s_waitcnt lgkmcnt(6)
	v_mfma_f32_16x16x32_bf16 v[66:69], v[210:213], v[110:113], v[66:69]
	ds_read_b128 v[210:213], v200 offset:60928
	s_waitcnt lgkmcnt(6)
	v_mfma_f32_16x16x32_bf16 v[62:65], v[214:217], v[110:113], v[62:65]
	ds_read_b128 v[214:217], v200 offset:65280
	s_waitcnt lgkmcnt(6)
	v_mfma_f32_16x16x32_bf16 v[58:61], v[228:231], v[110:113], v[58:61]
	ds_read_b128 v[228:231], v200 offset:64
	s_waitcnt lgkmcnt(6)
	v_mfma_f32_16x16x32_bf16 v[54:57], v[232:235], v[110:113], v[54:57]
	ds_read_b128 v[232:235], v200 offset:4416
	s_waitcnt lgkmcnt(6)
	v_mfma_f32_16x16x32_bf16 v[50:53], v[236:239], v[110:113], v[50:53]
	ds_read_b128 v[236:239], v200 offset:8768
	s_waitcnt lgkmcnt(6)
	v_mfma_f32_16x16x32_bf16 v[46:49], v[240:243], v[110:113], v[46:49]
	ds_read_b128 v[240:243], v200 offset:13120
	s_waitcnt lgkmcnt(6)
	v_mfma_f32_16x16x32_bf16 v[42:45], v[244:247], v[110:113], v[42:45]
	ds_read_b128 v[244:247], v200 offset:17472
	s_waitcnt lgkmcnt(6)
	v_mfma_f32_16x16x32_bf16 v[38:41], v[210:213], v[110:113], v[38:41]
	ds_read_b128 v[210:213], v200 offset:21824
	s_waitcnt lgkmcnt(6)
	v_mfma_f32_16x16x32_bf16 v[34:37], v[214:217], v[110:113], v[34:37]
	s_cbranch_scc0 .Lxa_aq_8_0
	v_lshl_add_u64 v[110:111], v[184:185], 0, s[10:11]
	global_load_dwordx4 v[110:113], v[110:111], off offset:-128
; #define MFMA16(b, a, c) __builtin_amdgcn_mfma_f32_16x16x32_bf16((b), (a), (c), 0, 0, 0)
; __device__ __forceinline__ void xattn_unit(LAS unsigned char* lds, int hd, int qt, const bf16_t* QX, const bf16_t* KX, const bf16_t* VX, bf16_t* O) {
;     ...
;         for (int ks = 0; ks < 4; ++ks) aq[ks] = *(const bf16x8*)(QX + trow * D + hd * XD + kc * 128 + 32 * ks + 8 * fq);
;         if (kc < 3) stage_load<NMEM, 128>(pf, KX + hd * XD + (kc + 1) * 128, D, tid);
;         __syncthreads();
; #pragma unroll
;         for (int ks = 0; ks < 4; ++ks)
; #pragma unroll
;             for (int j = 0; j < 16; ++j) S[j] = MFMA16(row_frag(X, (128 + 8) * 2, 16 * j, 32 * ks, lane), aq[ks], S[j]);
.Lxa_aq_8_0:
	ds_read_b128 v[214:217], v200 offset:26176
	s_waitcnt lgkmcnt(6)
	s_waitcnt vmcnt(10)
	v_mfma_f32_16x16x32_bf16 v[94:97], v[228:231], v[106:109], v[94:97]
	ds_read_b128 v[228:231], v200 offset:30528
	s_waitcnt lgkmcnt(6)
	v_mfma_f32_16x16x32_bf16 v[90:93], v[232:235], v[106:109], v[90:93]
	ds_read_b128 v[232:235], v200 offset:34880
	s_waitcnt lgkmcnt(6)
	v_mfma_f32_16x16x32_bf16 v[86:89], v[236:239], v[106:109], v[86:89]
	ds_read_b128 v[236:239], v200 offset:39232
	s_waitcnt lgkmcnt(6)
	v_mfma_f32_16x16x32_bf16 v[82:85], v[240:243], v[106:109], v[82:85]
	ds_read_b128 v[240:243], v200 offset:43584
	s_waitcnt lgkmcnt(6)
	v_mfma_f32_16x16x32_bf16 v[78:81], v[244:247], v[106:109], v[78:81]
	ds_read_b128 v[244:247], v200 offset:47936
	s_waitcnt lgkmcnt(6)
	v_mfma_f32_16x16x32_bf16 v[74:77], v[210:213], v[106:109], v[74:77]
	ds_read_b128 v[210:213], v200 offset:52288
	s_waitcnt lgkmcnt(6)
	v_mfma_f32_16x16x32_bf16 v[70:73], v[214:217], v[106:109], v[70:73]
	ds_read_b128 v[214:217], v200 offset:56640
	s_waitcnt lgkmcnt(6)
	v_mfma_f32_16x16x32_bf16 v[66:69], v[228:231], v[106:109], v[66:69]
	ds_read_b128 v[228:231], v200 offset:60992
	s_waitcnt lgkmcnt(6)
	v_mfma_f32_16x16x32_bf16 v[62:65], v[232:235], v[106:109], v[62:65]
	ds_read_b128 v[232:235], v200 offset:65344
	s_waitcnt lgkmcnt(6)
	v_mfma_f32_16x16x32_bf16 v[58:61], v[236:239], v[106:109], v[58:61]
	ds_read_b128 v[236:239], v200 offset:128
	s_waitcnt lgkmcnt(6)
	v_mfma_f32_16x16x32_bf16 v[54:57], v[240:243], v[106:109], v[54:57]
	ds_read_b128 v[240:243], v200 offset:4480
	s_waitcnt lgkmcnt(6)
	v_mfma_f32_16x16x32_bf16 v[50:53], v[244:247], v[106:109], v[50:53]
	ds_read_b128 v[244:247], v200 offset:8832
	s_waitcnt lgkmcnt(6)
	v_mfma_f32_16x16x32_bf16 v[46:49], v[210:213], v[106:109], v[46:49]
	ds_read_b128 v[210:213], v200 offset:13184
	s_waitcnt lgkmcnt(6)
	v_mfma_f32_16x16x32_bf16 v[42:45], v[214:217], v[106:109], v[42:45]
	ds_read_b128 v[214:217], v200 offset:17536
	s_waitcnt lgkmcnt(6)
	v_mfma_f32_16x16x32_bf16 v[38:41], v[228:231], v[106:109], v[38:41]
	ds_read_b128 v[228:231], v200 offset:21888
	s_waitcnt lgkmcnt(6)
	v_mfma_f32_16x16x32_bf16 v[34:37], v[232:235], v[106:109], v[34:37]
	s_cbranch_scc0 .Lxa_aq_8_1
	v_lshl_add_u64 v[106:107], v[184:185], 0, s[10:11]
	global_load_dwordx4 v[106:109], v[106:107], off offset:-64
.Lxa_aq_8_1:
	ds_read_b128 v[232:235], v200 offset:26240
	s_waitcnt lgkmcnt(6)
	s_waitcnt vmcnt(9)
	v_mfma_f32_16x16x32_bf16 v[94:97], v[236:239], v[102:105], v[94:97]
	ds_read_b128 v[236:239], v200 offset:30592
	s_waitcnt lgkmcnt(6)
	v_mfma_f32_16x16x32_bf16 v[90:93], v[240:243], v[102:105], v[90:93]
	ds_read_b128 v[240:243], v200 offset:34944
	s_waitcnt lgkmcnt(6)
	v_mfma_f32_16x16x32_bf16 v[86:89], v[244:247], v[102:105], v[86:89]
	ds_read_b128 v[244:247], v200 offset:39296
	s_waitcnt lgkmcnt(6)
	v_mfma_f32_16x16x32_bf16 v[82:85], v[210:213], v[102:105], v[82:85]
	ds_read_b128 v[210:213], v200 offset:43648
	s_waitcnt lgkmcnt(6)
	v_mfma_f32_16x16x32_bf16 v[78:81], v[214:217], v[102:105], v[78:81]
	ds_read_b128 v[214:217], v200 offset:48000
	s_waitcnt lgkmcnt(6)
	v_mfma_f32_16x16x32_bf16 v[74:77], v[228:231], v[102:105], v[74:77]
	ds_read_b128 v[228:231], v200 offset:52352
	s_waitcnt lgkmcnt(6)
	v_mfma_f32_16x16x32_bf16 v[70:73], v[232:235], v[102:105], v[70:73]
	ds_read_b128 v[232:235], v200 offset:56704
	s_waitcnt lgkmcnt(6)
	v_mfma_f32_16x16x32_bf16 v[66:69], v[236:239], v[102:105], v[66:69]
	ds_read_b128 v[236:239], v200 offset:61056
	s_waitcnt lgkmcnt(6)
	v_mfma_f32_16x16x32_bf16 v[62:65], v[240:243], v[102:105], v[62:65]
	ds_read_b128 v[240:243], v200 offset:65408
	s_waitcnt lgkmcnt(6)
	v_mfma_f32_16x16x32_bf16 v[58:61], v[244:247], v[102:105], v[58:61]
	ds_read_b128 v[244:247], v200 offset:192
	s_waitcnt lgkmcnt(6)
	v_mfma_f32_16x16x32_bf16 v[54:57], v[210:213], v[102:105], v[54:57]
	ds_read_b128 v[210:213], v200 offset:4544
	s_waitcnt lgkmcnt(6)
	v_mfma_f32_16x16x32_bf16 v[50:53], v[214:217], v[102:105], v[50:53]
	ds_read_b128 v[214:217], v200 offset:8896
	s_waitcnt lgkmcnt(6)
	v_mfma_f32_16x16x32_bf16 v[46:49], v[228:231], v[102:105], v[46:49]
	ds_read_b128 v[228:231], v200 offset:13248
	s_waitcnt lgkmcnt(6)
	v_mfma_f32_16x16x32_bf16 v[42:45], v[232:235], v[102:105], v[42:45]
	ds_read_b128 v[232:235], v200 offset:17600
	s_waitcnt lgkmcnt(6)
	v_mfma_f32_16x16x32_bf16 v[38:41], v[236:239], v[102:105], v[38:41]
	ds_read_b128 v[236:239], v200 offset:21952
	s_waitcnt lgkmcnt(6)
	v_mfma_f32_16x16x32_bf16 v[34:37], v[240:243], v[102:105], v[34:37]
	s_cbranch_scc0 .Lxa_aq_8_2
	v_lshl_add_u64 v[102:103], v[184:185], 0, s[10:11]
	global_load_dwordx4 v[102:105], v[102:103], off
; #define MFMA16(b, a, c) __builtin_amdgcn_mfma_f32_16x16x32_bf16((b), (a), (c), 0, 0, 0)
; __device__ __forceinline__ void xattn_unit(LAS unsigned char* lds, int hd, int qt, const bf16_t* QX, const bf16_t* KX, const bf16_t* VX, bf16_t* O) {
;     ...
;     for (int kc = 0; kc < 4; ++kc) {
;         __syncthreads();
;         stage_store<NMEM, 128, 8>(X, pf, tid);
;         bf16x8 aq[4];
; #pragma unroll
;         for (int ks = 0; ks < 4; ++ks) aq[ks] = *(const bf16x8*)(QX + trow * D + hd * XD + kc * 128 + 32 * ks + 8 * fq);
;         if (kc < 3) stage_load<NMEM, 128>(pf, KX + hd * XD + (kc + 1) * 128, D, tid);
;         __syncthreads();
; #pragma unroll
;         for (int ks = 0; ks < 4; ++ks)
; #pragma unroll
;             for (int j = 0; j < 16; ++j) S[j] = MFMA16(row_frag(X, (128 + 8) * 2, 16 * j, 32 * ks, lane), aq[ks], S[j]);
.Lxa_aq_8_2:
	ds_read_b128 v[240:243], v200 offset:26304
	s_waitcnt lgkmcnt(6)
	s_waitcnt vmcnt(8)
	v_mfma_f32_16x16x32_bf16 v[94:97], v[244:247], v[98:101], v[94:97]
	ds_read_b128 v[244:247], v200 offset:30656
	s_waitcnt lgkmcnt(6)
	v_mfma_f32_16x16x32_bf16 v[90:93], v[210:213], v[98:101], v[90:93]
	ds_read_b128 v[210:213], v200 offset:35008
	s_waitcnt lgkmcnt(6)
	v_mfma_f32_16x16x32_bf16 v[86:89], v[214:217], v[98:101], v[86:89]
	ds_read_b128 v[214:217], v200 offset:39360
	s_waitcnt lgkmcnt(6)
	v_mfma_f32_16x16x32_bf16 v[82:85], v[228:231], v[98:101], v[82:85]
	ds_read_b128 v[228:231], v200 offset:43712
	s_waitcnt lgkmcnt(6)
	v_mfma_f32_16x16x32_bf16 v[78:81], v[232:235], v[98:101], v[78:81]
	ds_read_b128 v[232:235], v200 offset:48064
	s_waitcnt lgkmcnt(6)
	v_mfma_f32_16x16x32_bf16 v[74:77], v[236:239], v[98:101], v[74:77]
	ds_read_b128 v[236:239], v200 offset:52416
	s_waitcnt lgkmcnt(6)
	v_mfma_f32_16x16x32_bf16 v[70:73], v[240:243], v[98:101], v[70:73]
	ds_read_b128 v[240:243], v200 offset:56768
	s_waitcnt lgkmcnt(6)
	v_mfma_f32_16x16x32_bf16 v[66:69], v[244:247], v[98:101], v[66:69]
	ds_read_b128 v[244:247], v200 offset:61120
	s_waitcnt lgkmcnt(6)
	v_mfma_f32_16x16x32_bf16 v[62:65], v[210:213], v[98:101], v[62:65]
	ds_read_b128 v[210:213], v200 offset:65472
	s_waitcnt lgkmcnt(6)
	v_mfma_f32_16x16x32_bf16 v[58:61], v[214:217], v[98:101], v[58:61]
	s_waitcnt lgkmcnt(5)
	v_mfma_f32_16x16x32_bf16 v[54:57], v[228:231], v[98:101], v[54:57]
	s_waitcnt lgkmcnt(4)
	v_mfma_f32_16x16x32_bf16 v[50:53], v[232:235], v[98:101], v[50:53]
	s_waitcnt lgkmcnt(3)
	v_mfma_f32_16x16x32_bf16 v[46:49], v[236:239], v[98:101], v[46:49]
	s_waitcnt lgkmcnt(2)
	v_mfma_f32_16x16x32_bf16 v[42:45], v[240:243], v[98:101], v[42:45]
	s_waitcnt lgkmcnt(1)
	v_mfma_f32_16x16x32_bf16 v[38:41], v[244:247], v[98:101], v[38:41]
	s_waitcnt lgkmcnt(0)
	v_mfma_f32_16x16x32_bf16 v[34:37], v[210:213], v[98:101], v[34:37]
	s_cbranch_scc0 .Lxa_aq_8_3
	v_lshl_add_u64 v[98:99], v[184:185], 0, s[10:11]
	global_load_dwordx4 v[98:101], v[98:99], off offset:64
.Lxa_aq_8_3:
	s_cbranch_scc0 .LBB0_982
.LBB0_980:
	s_barrier
	s_cmpk_eq_i32 s10, 0x300
	s_waitcnt vmcnt(11)
	ds_write_b128 v201, v[2:5]
	s_waitcnt vmcnt(10)
	ds_write_b128 v202, v[6:9]
	s_waitcnt vmcnt(9)
	ds_write_b128 v203, v[10:13]
	s_waitcnt vmcnt(8)
	ds_write_b128 v204, v[14:17]
	s_waitcnt vmcnt(7)
	ds_write_b128 v205, v[18:21]
	s_waitcnt vmcnt(6)
	ds_write_b128 v206, v[22:25]
	s_waitcnt vmcnt(5)
	ds_write_b128 v207, v[26:29]
	s_waitcnt vmcnt(4)
	ds_write_b128 v208, v[30:33]
	s_cbranch_scc1 .Lxa_last_0
	v_lshl_add_u64 v[2:3], v[180:181], 0, s[10:11]
	v_lshl_add_u64 v[6:7], v[182:183], 0, s[10:11]
	v_lshl_add_u64 v[10:11], v[186:187], 0, s[10:11]
	v_lshl_add_u64 v[14:15], v[196:197], 0, s[10:11]
	v_lshl_add_u64 v[18:19], v[194:195], 0, s[10:11]
	v_lshl_add_u64 v[22:23], v[192:193], 0, s[10:11]
	v_lshl_add_u64 v[26:27], v[190:191], 0, s[10:11]
	v_lshl_add_u64 v[30:31], v[188:189], 0, s[10:11]
	global_load_dwordx4 v[2:5], v[2:3], off
	s_nop 0
	global_load_dwordx4 v[6:9], v[6:7], off
	s_nop 0
	global_load_dwordx4 v[10:13], v[10:11], off
	s_nop 0
	global_load_dwordx4 v[14:17], v[14:15], off
	s_nop 0
	global_load_dwordx4 v[18:21], v[18:19], off
	s_nop 0
	global_load_dwordx4 v[22:25], v[22:23], off
	s_nop 0
	global_load_dwordx4 v[26:29], v[26:27], off
	s_nop 0
	global_load_dwordx4 v[30:33], v[30:31], off
	s_branch .LBB0_979

; #define LAS __attribute__((address_space(3)))
; __device__ __forceinline__ int fresh_tid() { int t = threadIdx.x; asm volatile("" : "+v"(t)); return t; }
; template <int ROWS, int COLS> __device__ __forceinline__ void stage_load(u32x4 (&v)[ROWS * (COLS / 8) / NTHR], const bf16_t* src, size_t ld, int tid) {
;     constexpr int CPR = COLS / 8, NI = ROWS * CPR / NTHR;
; #pragma unroll
;     for (int i = 0; i < NI; ++i) { const int idx = tid + i * NTHR, r = idx / CPR, c = idx % CPR; v[i] = *(const u32x4*)(src + (size_t)r * ld + c * 8); }
; }
; template <int ROWS, int COLS, int PAD> __device__ __forceinline__ void stage_store(LAS unsigned char* dst, const u32x4 (&v)[ROWS * (COLS / 8) / NTHR], int tid) {
;     constexpr int CPR = COLS / 8, NI = ROWS * CPR / NTHR, RS = (COLS + PAD) * 2;
; #pragma unroll
;     for (int i = 0; i < NI; ++i) { const int idx = tid + i * NTHR, r = idx / CPR, c = idx % CPR; *(LAS u32x4*)(dst + r * RS + c * 16) = v[i]; }
; }
; __device__ __forceinline__ void xattn_unit(LAS unsigned char* lds, int hd, int qt, const bf16_t* QX, const bf16_t* KX, const bf16_t* VX, bf16_t* O) {
;     ...
;     const int tid = fresh_tid(), lane = tid & 63, wave = __builtin_amdgcn_readfirstlane(tid >> 6), fr = lane & 15, fq = lane >> 4;
;     LAS unsigned char* X = lds; LAS unsigned char* Pw = lds + XBYTES + wave * 16 * PRS;
;     const size_t trow = (size_t)qt * 128 + 16 * wave + fr;
;     f32x4 S[16];
; #pragma unroll
;     for (int j = 0; j < 16; ++j) S[j] = (f32x4){0.f, 0.f, 0.f, 0.f};
;     u32x4 pf[8];
;     stage_load<NMEM, 128>(pf, KX + hd * XD, D, tid);
.LBB0_1813:
	v_mov_b32_e32 v198, v0
	s_lshl_b32 s12, s29, 1
	s_and_b32 s33, s12, 0xc00
	v_readfirstlane_b32 s13, v198
	s_ashr_i32 s12, s20, 2
	s_ashr_i32 s13, s13, 2
	s_and_b32 s15, s13, -16
	s_ashr_i32 s13, s12, 31
	s_ashr_i32 s14, s15, 31
	s_lshl_b64 s[12:13], s[12:13], 7
	s_waitcnt vmcnt(0)
	v_ashrrev_i32_e32 v2, 31, v198
	s_add_u32 s16, s12, s15
	v_lshrrev_b32_e32 v2, 28, v2
	s_addc_u32 s17, s13, s14
	s_lshl_b32 s12, s20, 9
	v_add_u32_e32 v2, v198, v2
	s_and_b32 s14, s12, 0x600
	v_ashrrev_i32_e32 v116, 4, v2
	v_and_b32_e32 v2, -16, v2
	s_lshl_b32 s12, s14, 1
	v_sub_u32_e32 v54, v198, v2
	s_add_u32 s12, s22, s12
	v_ashrrev_i32_e32 v117, 31, v116
	v_lshlrev_b32_e32 v126, 3, v54
	s_addc_u32 s13, s23, 0
	v_lshlrev_b64 v[124:125], 12, v[116:117]
	v_ashrrev_i32_e32 v127, 31, v126
	v_lshl_add_u64 v[2:3], s[12:13], 0, v[124:125]
	v_lshlrev_b64 v[34:35], 1, v[126:127]
	v_lshl_add_u64 v[10:11], v[2:3], 0, v[34:35]
	v_add_u32_e32 v2, 0x200, v198
	v_ashrrev_i32_e32 v3, 31, v2
	v_lshrrev_b32_e32 v3, 28, v3
	v_add_u32_e32 v3, v2, v3
	v_ashrrev_i32_e32 v118, 4, v3
	v_and_b32_e32 v3, -16, v3
	v_sub_u32_e32 v55, v2, v3
	v_ashrrev_i32_e32 v119, 31, v118
	v_lshlrev_b32_e32 v132, 3, v55
	v_lshlrev_b64 v[130:131], 12, v[118:119]
	v_ashrrev_i32_e32 v133, 31, v132
	v_lshl_add_u64 v[2:3], s[12:13], 0, v[130:131]
	v_lshlrev_b64 v[36:37], 1, v[132:133]
	v_lshl_add_u64 v[12:13], v[2:3], 0, v[36:37]
	global_load_dwordx4 v[2:5], v[10:11], off
	global_load_dwordx4 v[6:9], v[12:13], off
	v_add_u32_e32 v10, 0x400, v198
	v_ashrrev_i32_e32 v11, 31, v10
	v_lshrrev_b32_e32 v11, 28, v11
	v_add_u32_e32 v11, v10, v11
	v_ashrrev_i32_e32 v120, 4, v11
	v_and_b32_e32 v11, -16, v11
	v_sub_u32_e32 v56, v10, v11
	v_ashrrev_i32_e32 v121, 31, v120
	v_lshlrev_b32_e32 v138, 3, v56
	v_lshlrev_b64 v[136:137], 12, v[120:121]
	v_ashrrev_i32_e32 v139, 31, v138
	v_lshl_add_u64 v[10:11], s[12:13], 0, v[136:137]
	v_lshlrev_b64 v[38:39], 1, v[138:139]
	v_lshl_add_u64 v[18:19], v[10:11], 0, v[38:39]
	v_add_u32_e32 v10, 0x600, v198
	v_ashrrev_i32_e32 v11, 31, v10
	v_lshrrev_b32_e32 v11, 28, v11
	v_add_u32_e32 v11, v10, v11
	v_ashrrev_i32_e32 v122, 4, v11
	v_and_b32_e32 v11, -16, v11
	v_sub_u32_e32 v57, v10, v11
	v_ashrrev_i32_e32 v123, 31, v122
	v_lshlrev_b32_e32 v144, 3, v57
	v_lshlrev_b64 v[142:143], 12, v[122:123]
	v_ashrrev_i32_e32 v145, 31, v144
	v_lshl_add_u64 v[10:11], s[12:13], 0, v[142:143]
	v_lshlrev_b64 v[40:41], 1, v[144:145]
	v_lshl_add_u64 v[20:21], v[10:11], 0, v[40:41]
	global_load_dwordx4 v[10:13], v[18:19], off
	global_load_dwordx4 v[14:17], v[20:21], off
	v_add_u32_e32 v18, 0x800, v198
	v_ashrrev_i32_e32 v19, 31, v18
	v_lshrrev_b32_e32 v19, 28, v19
	v_add_u32_e32 v19, v18, v19
	v_ashrrev_i32_e32 v128, 4, v19
	v_and_b32_e32 v19, -16, v19
	v_sub_u32_e32 v58, v18, v19
	v_ashrrev_i32_e32 v129, 31, v128
	v_lshlrev_b32_e32 v150, 3, v58
	v_lshlrev_b64 v[148:149], 12, v[128:129]
	v_ashrrev_i32_e32 v151, 31, v150
	v_lshl_add_u64 v[18:19], s[12:13], 0, v[148:149]
	v_lshlrev_b64 v[42:43], 1, v[150:151]
	v_lshl_add_u64 v[26:27], v[18:19], 0, v[42:43]
	v_add_u32_e32 v18, 0xa00, v198
	v_ashrrev_i32_e32 v19, 31, v18
	v_lshrrev_b32_e32 v19, 28, v19
	v_add_u32_e32 v19, v18, v19
	v_ashrrev_i32_e32 v134, 4, v19
	v_and_b32_e32 v19, -16, v19
	v_sub_u32_e32 v59, v18, v19
	v_ashrrev_i32_e32 v135, 31, v134
	v_lshlrev_b32_e32 v158, 3, v59
	v_lshlrev_b64 v[156:157], 12, v[134:135]
	v_ashrrev_i32_e32 v159, 31, v158
	v_lshl_add_u64 v[18:19], s[12:13], 0, v[156:157]
	v_lshlrev_b64 v[44:45], 1, v[158:159]
	v_lshl_add_u64 v[28:29], v[18:19], 0, v[44:45]
	global_load_dwordx4 v[18:21], v[26:27], off
	global_load_dwordx4 v[22:25], v[28:29], off
	v_add_u32_e32 v26, 0xc00, v198
	v_ashrrev_i32_e32 v27, 31, v26
	v_lshrrev_b32_e32 v27, 28, v27
	v_add_u32_e32 v27, v26, v27
	v_ashrrev_i32_e32 v140, 4, v27
	v_and_b32_e32 v27, -16, v27
	v_sub_u32_e32 v60, v26, v27
	v_ashrrev_i32_e32 v141, 31, v140
	v_lshlrev_b32_e32 v164, 3, v60
	v_lshlrev_b64 v[162:163], 12, v[140:141]
	v_ashrrev_i32_e32 v165, 31, v164
	v_lshl_add_u64 v[26:27], s[12:13], 0, v[162:163]
	v_lshlrev_b64 v[46:47], 1, v[164:165]
	v_lshl_add_u64 v[48:49], v[26:27], 0, v[46:47]
	v_add_u32_e32 v26, 0xe00, v198
	v_ashrrev_i32_e32 v27, 31, v26
	v_lshrrev_b32_e32 v27, 28, v27
	v_add_u32_e32 v27, v26, v27
	v_ashrrev_i32_e32 v146, 4, v27
	v_and_b32_e32 v27, -16, v27
	v_sub_u32_e32 v61, v26, v27
	v_ashrrev_i32_e32 v147, 31, v146
	v_lshlrev_b32_e32 v176, 3, v61
	v_lshlrev_b64 v[174:175], 12, v[146:147]
	v_ashrrev_i32_e32 v177, 31, v176
	v_lshl_add_u64 v[26:27], s[12:13], 0, v[174:175]
	v_lshlrev_b64 v[50:51], 1, v[176:177]
	v_lshl_add_u64 v[52:53], v[26:27], 0, v[50:51]
	global_load_dwordx4 v[26:29], v[48:49], off
	global_load_dwordx4 v[30:33], v[52:53], off
	v_mul_lo_u32 v48, v116, s31
	v_add_u32_e32 v52, s3, v48
	v_mul_lo_u32 v48, v118, s31
	v_add_u32_e32 v53, s3, v48
	v_mul_lo_u32 v48, v120, s31
	v_lshlrev_b32_e32 v117, 4, v54
	v_add_u32_e32 v54, s3, v48
	v_mul_lo_u32 v48, v122, s31
	v_lshlrev_b32_e32 v119, 4, v55
	v_add_u32_e32 v55, s3, v48
	v_mul_lo_u32 v48, v128, s31
	v_lshlrev_b32_e32 v121, 4, v56
	v_add_u32_e32 v56, s3, v48
	v_mul_lo_u32 v48, v134, s31
	v_lshlrev_b32_e32 v123, 4, v57
	v_add_u32_e32 v57, s3, v48
	v_mul_lo_u32 v48, v140, s31
	v_and_b32_e32 v114, 15, v198
	v_lshlrev_b32_e32 v129, 4, v58
	v_add_u32_e32 v58, s3, v48
	v_mul_lo_u32 v48, v146, s31
	v_lshlrev_b32_e32 v135, 4, v59
	v_add_u32_e32 v59, s3, v48
	v_and_b32_e32 v199, 48, v198
	v_mul_u32_u24_e32 v48, 0x110, v114
	v_add3_u32 v200, s3, v199, v48
	v_or_b32_e32 v48, s33, v124
	v_mov_b32_e32 v49, v125
	v_lshl_add_u64 v[152:153], v[48:49], 0, v[34:35]
	v_or_b32_e32 v34, s33, v130
; #define MFMA16(b, a, c) __builtin_amdgcn_mfma_f32_16x16x32_bf16((b), (a), (c), 0, 0, 0)
; __device__ __forceinline__ void xattn_unit(LAS unsigned char* lds, int hd, int qt, const bf16_t* QX, const bf16_t* KX, const bf16_t* VX, bf16_t* O) {
;     ...
;     f32x4 S[16];
; #pragma unroll
;     for (int j = 0; j < 16; ++j) S[j] = (f32x4){0.f, 0.f, 0.f, 0.f};
;     u32x4 pf[8];
;     stage_load<NMEM, 128>(pf, KX + hd * XD, D, tid);
; #pragma unroll 1
;     for (int kc = 0; kc < 4; ++kc) {
;         __syncthreads();
;         stage_store<NMEM, 128, 8>(X, pf, tid);
;         bf16x8 aq[4];
; #pragma unroll
;         for (int ks = 0; ks < 4; ++ks) aq[ks] = *(const bf16x8*)(QX + trow * D + hd * XD + kc * 128 + 32 * ks + 8 * fq);
;         if (kc < 3) stage_load<NMEM, 128>(pf, KX + hd * XD + (kc + 1) * 128, D, tid);
;         __syncthreads();
; #pragma unroll
;         for (int ks = 0; ks < 4; ++ks)
; #pragma unroll
;             for (int j = 0; j < 16; ++j) S[j] = MFMA16(row_frag(X, (128 + 8) * 2, 16 * j, 32 * ks, lane), aq[ks], S[j]);
	v_mov_b32_e32 v35, v131
	v_lshl_add_u64 v[154:155], v[34:35], 0, v[36:37]
	v_or_b32_e32 v34, s16, v114
	v_mov_b32_e32 v35, s17
	v_lshlrev_b64 v[34:35], 12, v[34:35]
	v_or3_b32 v34, v34, s33, v199
	v_lshl_add_u64 v[184:185], s[8:9], 0, v[34:35]
	v_or_b32_e32 v34, s33, v136
	v_mov_b32_e32 v35, v137
	v_lshl_add_u64 v[160:161], v[34:35], 0, v[38:39]
	v_or_b32_e32 v34, s33, v174
	v_mov_b32_e32 v35, v175
	v_lshl_add_u64 v[166:167], v[34:35], 0, v[50:51]
	v_or_b32_e32 v34, s33, v162
	v_mov_b32_e32 v35, v163
	v_lshl_add_u64 v[168:169], v[34:35], 0, v[46:47]
	v_or_b32_e32 v34, s33, v156
	v_mov_b32_e32 v35, v157
	v_lshl_add_u64 v[170:171], v[34:35], 0, v[44:45]
	v_or_b32_e32 v34, s33, v148
	v_mov_b32_e32 v35, v149
	v_lshl_add_u64 v[172:173], v[34:35], 0, v[42:43]
	v_or_b32_e32 v34, s33, v142
	v_mov_b32_e32 v35, v143
	v_lshlrev_b32_e32 v141, 4, v60
	v_lshlrev_b32_e32 v147, 4, v61
	v_lshl_add_u64 v[178:179], v[34:35], 0, v[40:41]
	v_lshl_add_u64 v[180:181], s[6:7], 0, v[152:153]
	v_lshl_add_u64 v[182:183], s[6:7], 0, v[154:155]
	v_lshl_add_u64 v[186:187], s[6:7], 0, v[160:161]
	v_lshl_add_u64 v[188:189], s[6:7], 0, v[166:167]
	v_lshl_add_u64 v[190:191], s[6:7], 0, v[168:169]
	v_lshl_add_u64 v[192:193], s[6:7], 0, v[170:171]
	v_lshl_add_u64 v[194:195], s[6:7], 0, v[172:173]
	v_lshl_add_u64 v[196:197], s[6:7], 0, v[178:179]
	s_mov_b64 s[12:13], 0
	v_add_u32_e32 v201, v52, v117
	v_add_u32_e32 v202, v53, v119
	v_add_u32_e32 v203, v54, v121
	v_add_u32_e32 v204, v55, v123
	v_add_u32_e32 v205, v56, v129
	v_add_u32_e32 v206, v57, v135
	v_add_u32_e32 v207, v58, v141
	v_add_u32_e32 v208, v59, v147
	v_mov_b32_e32 v82, 0
	v_mov_b32_e32 v83, v115
	v_mov_b32_e32 v84, v115
	v_mov_b32_e32 v85, v115
	v_mov_b32_e32 v86, 0
	v_mov_b32_e32 v87, v115
	v_mov_b32_e32 v88, v115
	v_mov_b32_e32 v89, v115
	v_mov_b32_e32 v90, 0
	v_mov_b32_e32 v91, v115
	v_mov_b32_e32 v92, v115
	v_mov_b32_e32 v93, v115
	v_mov_b32_e32 v94, 0
	v_mov_b32_e32 v95, v115
	v_mov_b32_e32 v96, v115
	v_mov_b32_e32 v97, v115
	v_mov_b32_e32 v78, 0
	v_mov_b32_e32 v79, v115
	v_mov_b32_e32 v80, v115
	v_mov_b32_e32 v81, v115
	v_mov_b32_e32 v74, 0
	v_mov_b32_e32 v75, v115
	v_mov_b32_e32 v76, v115
	v_mov_b32_e32 v77, v115
	v_mov_b32_e32 v70, 0
	v_mov_b32_e32 v71, v115
	v_mov_b32_e32 v72, v115
	v_mov_b32_e32 v73, v115
	v_mov_b32_e32 v66, 0
	v_mov_b32_e32 v67, v115
	v_mov_b32_e32 v68, v115
	v_mov_b32_e32 v69, v115
	v_mov_b32_e32 v62, 0
	v_mov_b32_e32 v63, v115
	v_mov_b32_e32 v64, v115
	v_mov_b32_e32 v65, v115
	v_mov_b32_e32 v58, 0
	v_mov_b32_e32 v59, v115
	v_mov_b32_e32 v60, v115
	v_mov_b32_e32 v61, v115
	v_mov_b32_e32 v54, 0
	v_mov_b32_e32 v55, v115
	v_mov_b32_e32 v56, v115
	v_mov_b32_e32 v57, v115
	v_mov_b32_e32 v50, 0
	v_mov_b32_e32 v51, v115
	v_mov_b32_e32 v52, v115
	v_mov_b32_e32 v53, v115
	v_mov_b32_e32 v46, 0
	v_mov_b32_e32 v47, v115
	v_mov_b32_e32 v48, v115
	v_mov_b32_e32 v49, v115
	v_mov_b32_e32 v42, 0
	v_mov_b32_e32 v43, v115
	v_mov_b32_e32 v44, v115
	v_mov_b32_e32 v45, v115
	v_mov_b32_e32 v38, 0
	v_mov_b32_e32 v39, v115
	v_mov_b32_e32 v40, v115
	v_mov_b32_e32 v41, v115
	v_mov_b32_e32 v34, 0
	v_mov_b32_e32 v35, v115
	v_mov_b32_e32 v36, v115
	v_mov_b32_e32 v37, v115
	v_lshl_add_u64 v[98:99], v[184:185], 0, s[12:13]
	global_load_dwordx4 v[110:113], v[98:99], off offset:-128
	global_load_dwordx4 v[106:109], v[98:99], off offset:-64
	global_load_dwordx4 v[102:105], v[98:99], off
	s_nop 0
	global_load_dwordx4 v[98:101], v[98:99], off offset:64
	s_branch .LBB0_1815
.LBB0_1814:
	s_waitcnt lgkmcnt(0)
	s_barrier
	s_add_u32 s12, s12, 0x100
	s_addc_u32 s13, s13, 0
	s_cmpk_lg_i32 s12, 0x400
	ds_read_b128 v[210:213], v200
	ds_read_b128 v[214:217], v200 offset:4352
	ds_read_b128 v[228:231], v200 offset:8704
	ds_read_b128 v[232:235], v200 offset:13056
	ds_read_b128 v[236:239], v200 offset:17408
	ds_read_b128 v[240:243], v200 offset:21760
	ds_read_b128 v[244:247], v200 offset:26112
	s_waitcnt lgkmcnt(6)
	s_waitcnt vmcnt(11)
	v_mfma_f32_16x16x32_bf16 v[94:97], v[210:213], v[110:113], v[94:97]
	ds_read_b128 v[210:213], v200 offset:30464
	s_waitcnt lgkmcnt(6)
	v_mfma_f32_16x16x32_bf16 v[90:93], v[214:217], v[110:113], v[90:93]
	ds_read_b128 v[214:217], v200 offset:34816
	s_waitcnt lgkmcnt(6)
	v_mfma_f32_16x16x32_bf16 v[86:89], v[228:231], v[110:113], v[86:89]
	ds_read_b128 v[228:231], v200 offset:39168
	s_waitcnt lgkmcnt(6)
	v_mfma_f32_16x16x32_bf16 v[82:85], v[232:235], v[110:113], v[82:85]
	ds_read_b128 v[232:235], v200 offset:43520
	s_waitcnt lgkmcnt(6)
	v_mfma_f32_16x16x32_bf16 v[78:81], v[236:239], v[110:113], v[78:81]
	ds_read_b128 v[236:239], v200 offset:47872
	s_waitcnt lgkmcnt(6)
	v_mfma_f32_16x16x32_bf16 v[74:77], v[240:243], v[110:113], v[74:77]
	ds_read_b128 v[240:243], v200 offset:52224
	s_waitcnt lgkmcnt(6)
	v_mfma_f32_16x16x32_bf16 v[70:73], v[244:247], v[110:113], v[70:73]
	ds_read_b128 v[244:247], v200 offset:56576
	s_waitcnt lgkmcnt(6)
	v_mfma_f32_16x16x32_bf16 v[66:69], v[210:213], v[110:113], v[66:69]
	ds_read_b128 v[210:213], v200 offset:60928
	s_waitcnt lgkmcnt(6)
	v_mfma_f32_16x16x32_bf16 v[62:65], v[214:217], v[110:113], v[62:65]
	ds_read_b128 v[214:217], v200 offset:65280
	s_waitcnt lgkmcnt(6)
	v_mfma_f32_16x16x32_bf16 v[58:61], v[228:231], v[110:113], v[58:61]
	ds_read_b128 v[228:231], v200 offset:64
	s_waitcnt lgkmcnt(6)
	v_mfma_f32_16x16x32_bf16 v[54:57], v[232:235], v[110:113], v[54:57]
	ds_read_b128 v[232:235], v200 offset:4416
	s_waitcnt lgkmcnt(6)
	v_mfma_f32_16x16x32_bf16 v[50:53], v[236:239], v[110:113], v[50:53]
	ds_read_b128 v[236:239], v200 offset:8768
	s_waitcnt lgkmcnt(6)
	v_mfma_f32_16x16x32_bf16 v[46:49], v[240:243], v[110:113], v[46:49]
	ds_read_b128 v[240:243], v200 offset:13120
	s_waitcnt lgkmcnt(6)
	v_mfma_f32_16x16x32_bf16 v[42:45], v[244:247], v[110:113], v[42:45]
	ds_read_b128 v[244:247], v200 offset:17472
	s_waitcnt lgkmcnt(6)
	v_mfma_f32_16x16x32_bf16 v[38:41], v[210:213], v[110:113], v[38:41]
	ds_read_b128 v[210:213], v200 offset:21824
	s_waitcnt lgkmcnt(6)
	v_mfma_f32_16x16x32_bf16 v[34:37], v[214:217], v[110:113], v[34:37]
	s_cbranch_scc0 .Lxa_aq_21_0
	v_lshl_add_u64 v[110:111], v[184:185], 0, s[12:13]
	global_load_dwordx4 v[110:113], v[110:111], off offset:-128
; #define MFMA16(b, a, c) __builtin_amdgcn_mfma_f32_16x16x32_bf16((b), (a), (c), 0, 0, 0)
; __device__ __forceinline__ void xattn_unit(LAS unsigned char* lds, int hd, int qt, const bf16_t* QX, const bf16_t* KX, const bf16_t* VX, bf16_t* O) {
;     ...
;         for (int ks = 0; ks < 4; ++ks) aq[ks] = *(const bf16x8*)(QX + trow * D + hd * XD + kc * 128 + 32 * ks + 8 * fq);
;         if (kc < 3) stage_load<NMEM, 128>(pf, KX + hd * XD + (kc + 1) * 128, D, tid);
;         __syncthreads();
; #pragma unroll
;         for (int ks = 0; ks < 4; ++ks)
; #pragma unroll
;             for (int j = 0; j < 16; ++j) S[j] = MFMA16(row_frag(X, (128 + 8) * 2, 16 * j, 32 * ks, lane), aq[ks], S[j]);
.Lxa_aq_21_0:
	ds_read_b128 v[214:217], v200 offset:26176
	s_waitcnt lgkmcnt(6)
	s_waitcnt vmcnt(10)
	v_mfma_f32_16x16x32_bf16 v[94:97], v[228:231], v[106:109], v[94:97]
	ds_read_b128 v[228:231], v200 offset:30528
	s_waitcnt lgkmcnt(6)
	v_mfma_f32_16x16x32_bf16 v[90:93], v[232:235], v[106:109], v[90:93]
	ds_read_b128 v[232:235], v200 offset:34880
	s_waitcnt lgkmcnt(6)
	v_mfma_f32_16x16x32_bf16 v[86:89], v[236:239], v[106:109], v[86:89]
	ds_read_b128 v[236:239], v200 offset:39232
	s_waitcnt lgkmcnt(6)
	v_mfma_f32_16x16x32_bf16 v[82:85], v[240:243], v[106:109], v[82:85]
	ds_read_b128 v[240:243], v200 offset:43584
	s_waitcnt lgkmcnt(6)
	v_mfma_f32_16x16x32_bf16 v[78:81], v[244:247], v[106:109], v[78:81]
	ds_read_b128 v[244:247], v200 offset:47936
	s_waitcnt lgkmcnt(6)
	v_mfma_f32_16x16x32_bf16 v[74:77], v[210:213], v[106:109], v[74:77]
	ds_read_b128 v[210:213], v200 offset:52288
	s_waitcnt lgkmcnt(6)
	v_mfma_f32_16x16x32_bf16 v[70:73], v[214:217], v[106:109], v[70:73]
	ds_read_b128 v[214:217], v200 offset:56640
	s_waitcnt lgkmcnt(6)
	v_mfma_f32_16x16x32_bf16 v[66:69], v[228:231], v[106:109], v[66:69]
	ds_read_b128 v[228:231], v200 offset:60992
	s_waitcnt lgkmcnt(6)
	v_mfma_f32_16x16x32_bf16 v[62:65], v[232:235], v[106:109], v[62:65]
	ds_read_b128 v[232:235], v200 offset:65344
	s_waitcnt lgkmcnt(6)
	v_mfma_f32_16x16x32_bf16 v[58:61], v[236:239], v[106:109], v[58:61]
	ds_read_b128 v[236:239], v200 offset:128
	s_waitcnt lgkmcnt(6)
	v_mfma_f32_16x16x32_bf16 v[54:57], v[240:243], v[106:109], v[54:57]
	ds_read_b128 v[240:243], v200 offset:4480
	s_waitcnt lgkmcnt(6)
	v_mfma_f32_16x16x32_bf16 v[50:53], v[244:247], v[106:109], v[50:53]
	ds_read_b128 v[244:247], v200 offset:8832
	s_waitcnt lgkmcnt(6)
	v_mfma_f32_16x16x32_bf16 v[46:49], v[210:213], v[106:109], v[46:49]
	ds_read_b128 v[210:213], v200 offset:13184
	s_waitcnt lgkmcnt(6)
	v_mfma_f32_16x16x32_bf16 v[42:45], v[214:217], v[106:109], v[42:45]
	ds_read_b128 v[214:217], v200 offset:17536
	s_waitcnt lgkmcnt(6)
	v_mfma_f32_16x16x32_bf16 v[38:41], v[228:231], v[106:109], v[38:41]
	ds_read_b128 v[228:231], v200 offset:21888
	s_waitcnt lgkmcnt(6)
	v_mfma_f32_16x16x32_bf16 v[34:37], v[232:235], v[106:109], v[34:37]
	s_cbranch_scc0 .Lxa_aq_21_1
	v_lshl_add_u64 v[106:107], v[184:185], 0, s[12:13]
	global_load_dwordx4 v[106:109], v[106:107], off offset:-64
.Lxa_aq_21_1:
	ds_read_b128 v[232:235], v200 offset:26240
	s_waitcnt lgkmcnt(6)
	s_waitcnt vmcnt(9)
	v_mfma_f32_16x16x32_bf16 v[94:97], v[236:239], v[102:105], v[94:97]
	ds_read_b128 v[236:239], v200 offset:30592
	s_waitcnt lgkmcnt(6)
	v_mfma_f32_16x16x32_bf16 v[90:93], v[240:243], v[102:105], v[90:93]
	ds_read_b128 v[240:243], v200 offset:34944
	s_waitcnt lgkmcnt(6)
	v_mfma_f32_16x16x32_bf16 v[86:89], v[244:247], v[102:105], v[86:89]
	ds_read_b128 v[244:247], v200 offset:39296
	s_waitcnt lgkmcnt(6)
	v_mfma_f32_16x16x32_bf16 v[82:85], v[210:213], v[102:105], v[82:85]
	ds_read_b128 v[210:213], v200 offset:43648
	s_waitcnt lgkmcnt(6)
	v_mfma_f32_16x16x32_bf16 v[78:81], v[214:217], v[102:105], v[78:81]
	ds_read_b128 v[214:217], v200 offset:48000
	s_waitcnt lgkmcnt(6)
	v_mfma_f32_16x16x32_bf16 v[74:77], v[228:231], v[102:105], v[74:77]
	ds_read_b128 v[228:231], v200 offset:52352
	s_waitcnt lgkmcnt(6)
	v_mfma_f32_16x16x32_bf16 v[70:73], v[232:235], v[102:105], v[70:73]
	ds_read_b128 v[232:235], v200 offset:56704
	s_waitcnt lgkmcnt(6)
	v_mfma_f32_16x16x32_bf16 v[66:69], v[236:239], v[102:105], v[66:69]
	ds_read_b128 v[236:239], v200 offset:61056
	s_waitcnt lgkmcnt(6)
	v_mfma_f32_16x16x32_bf16 v[62:65], v[240:243], v[102:105], v[62:65]
	ds_read_b128 v[240:243], v200 offset:65408
	s_waitcnt lgkmcnt(6)
	v_mfma_f32_16x16x32_bf16 v[58:61], v[244:247], v[102:105], v[58:61]
	ds_read_b128 v[244:247], v200 offset:192
	s_waitcnt lgkmcnt(6)
	v_mfma_f32_16x16x32_bf16 v[54:57], v[210:213], v[102:105], v[54:57]
	ds_read_b128 v[210:213], v200 offset:4544
	s_waitcnt lgkmcnt(6)
	v_mfma_f32_16x16x32_bf16 v[50:53], v[214:217], v[102:105], v[50:53]
	ds_read_b128 v[214:217], v200 offset:8896
	s_waitcnt lgkmcnt(6)
	v_mfma_f32_16x16x32_bf16 v[46:49], v[228:231], v[102:105], v[46:49]
	ds_read_b128 v[228:231], v200 offset:13248
	s_waitcnt lgkmcnt(6)
	v_mfma_f32_16x16x32_bf16 v[42:45], v[232:235], v[102:105], v[42:45]
	ds_read_b128 v[232:235], v200 offset:17600
	s_waitcnt lgkmcnt(6)
	v_mfma_f32_16x16x32_bf16 v[38:41], v[236:239], v[102:105], v[38:41]
	ds_read_b128 v[236:239], v200 offset:21952
	s_waitcnt lgkmcnt(6)
	v_mfma_f32_16x16x32_bf16 v[34:37], v[240:243], v[102:105], v[34:37]
	s_cbranch_scc0 .Lxa_aq_21_2
	v_lshl_add_u64 v[102:103], v[184:185], 0, s[12:13]
	global_load_dwordx4 v[102:105], v[102:103], off
.Lxa_aq_21_2:
	ds_read_b128 v[240:243], v200 offset:26304
	s_waitcnt lgkmcnt(6)
	s_waitcnt vmcnt(8)
	v_mfma_f32_16x16x32_bf16 v[94:97], v[244:247], v[98:101], v[94:97]
	ds_read_b128 v[244:247], v200 offset:30656
	s_waitcnt lgkmcnt(6)
	v_mfma_f32_16x16x32_bf16 v[90:93], v[210:213], v[98:101], v[90:93]
	ds_read_b128 v[210:213], v200 offset:35008
	s_waitcnt lgkmcnt(6)
	v_mfma_f32_16x16x32_bf16 v[86:89], v[214:217], v[98:101], v[86:89]
	ds_read_b128 v[214:217], v200 offset:39360
	s_waitcnt lgkmcnt(6)
	v_mfma_f32_16x16x32_bf16 v[82:85], v[228:231], v[98:101], v[82:85]
	ds_read_b128 v[228:231], v200 offset:43712
	s_waitcnt lgkmcnt(6)
	v_mfma_f32_16x16x32_bf16 v[78:81], v[232:235], v[98:101], v[78:81]
	ds_read_b128 v[232:235], v200 offset:48064
	s_waitcnt lgkmcnt(6)
	v_mfma_f32_16x16x32_bf16 v[74:77], v[236:239], v[98:101], v[74:77]
	ds_read_b128 v[236:239], v200 offset:52416
	s_waitcnt lgkmcnt(6)
	v_mfma_f32_16x16x32_bf16 v[70:73], v[240:243], v[98:101], v[70:73]
	ds_read_b128 v[240:243], v200 offset:56768
	s_waitcnt lgkmcnt(6)
	v_mfma_f32_16x16x32_bf16 v[66:69], v[244:247], v[98:101], v[66:69]
	ds_read_b128 v[244:247], v200 offset:61120
	s_waitcnt lgkmcnt(6)
	v_mfma_f32_16x16x32_bf16 v[62:65], v[210:213], v[98:101], v[62:65]
	ds_read_b128 v[210:213], v200 offset:65472
	s_waitcnt lgkmcnt(6)
	v_mfma_f32_16x16x32_bf16 v[58:61], v[214:217], v[98:101], v[58:61]
	s_waitcnt lgkmcnt(5)
	v_mfma_f32_16x16x32_bf16 v[54:57], v[228:231], v[98:101], v[54:57]
	s_waitcnt lgkmcnt(4)
	v_mfma_f32_16x16x32_bf16 v[50:53], v[232:235], v[98:101], v[50:53]
	s_waitcnt lgkmcnt(3)
	v_mfma_f32_16x16x32_bf16 v[46:49], v[236:239], v[98:101], v[46:49]
	s_waitcnt lgkmcnt(2)
	v_mfma_f32_16x16x32_bf16 v[42:45], v[240:243], v[98:101], v[42:45]
	s_waitcnt lgkmcnt(1)
	v_mfma_f32_16x16x32_bf16 v[38:41], v[244:247], v[98:101], v[38:41]
	s_waitcnt lgkmcnt(0)
	v_mfma_f32_16x16x32_bf16 v[34:37], v[210:213], v[98:101], v[34:37]
	s_cbranch_scc0 .Lxa_aq_21_3
	v_lshl_add_u64 v[98:99], v[184:185], 0, s[12:13]
	global_load_dwordx4 v[98:101], v[98:99], off offset:64

; __device__ __forceinline__ void xattn_unit(LAS unsigned char* lds, int hd, int qt, const bf16_t* QX, const bf16_t* KX, const bf16_t* VX, bf16_t* O) {
;     ...
;     for (int kc = 0; kc < 4; ++kc) {
;         __syncthreads();
;         stage_store<NMEM, 128, 8>(X, pf, tid);
;         bf16x8 aq[4];
; #pragma unroll
;         for (int ks = 0; ks < 4; ++ks) aq[ks] = *(const bf16x8*)(QX + trow * D + hd * XD + kc * 128 + 32 * ks + 8 * fq);
;         if (kc < 3) stage_load<NMEM, 128>(pf, KX + hd * XD + (kc + 1) * 128, D, tid);
.LBB0_1815:
	s_barrier
	s_cmpk_eq_i32 s12, 0x300
	s_waitcnt vmcnt(11)
	ds_write_b128 v201, v[2:5]
	s_waitcnt vmcnt(10)
	ds_write_b128 v202, v[6:9]
	s_waitcnt vmcnt(9)
	ds_write_b128 v203, v[10:13]
	s_waitcnt vmcnt(8)
	ds_write_b128 v204, v[14:17]
	s_waitcnt vmcnt(7)
	ds_write_b128 v205, v[18:21]
	s_waitcnt vmcnt(6)
	ds_write_b128 v206, v[22:25]
	s_waitcnt vmcnt(5)
	ds_write_b128 v207, v[26:29]
	s_waitcnt vmcnt(4)
	ds_write_b128 v208, v[30:33]
	s_cbranch_scc1 .Lxa_last_1
	v_lshl_add_u64 v[2:3], v[180:181], 0, s[12:13]
	v_lshl_add_u64 v[6:7], v[182:183], 0, s[12:13]
	v_lshl_add_u64 v[10:11], v[186:187], 0, s[12:13]
	v_lshl_add_u64 v[14:15], v[196:197], 0, s[12:13]
	v_lshl_add_u64 v[18:19], v[194:195], 0, s[12:13]
	v_lshl_add_u64 v[22:23], v[192:193], 0, s[12:13]
	v_lshl_add_u64 v[26:27], v[190:191], 0, s[12:13]
	v_lshl_add_u64 v[30:31], v[188:189], 0, s[12:13]
	global_load_dwordx4 v[2:5], v[2:3], off
	s_nop 0
	global_load_dwordx4 v[6:9], v[6:7], off
	s_nop 0
	global_load_dwordx4 v[10:13], v[10:11], off
	s_nop 0
	global_load_dwordx4 v[14:17], v[14:15], off
	s_nop 0
	global_load_dwordx4 v[18:21], v[18:19], off
	s_nop 0
	global_load_dwordx4 v[22:25], v[22:23], off
	s_nop 0
	global_load_dwordx4 v[26:29], v[26:27], off
	s_nop 0
	global_load_dwordx4 v[30:33], v[30:31], off
	s_branch .LBB0_1814
